# stagger WG start by bx>>3 (0-4.8us) in G3 and G5 only, where delayed WGs have one fewer GEMM unit
# speedup vs baseline: 1.0060x; 1.0060x over previous
; template <class Epi, class Sched, bool ALIGN_EPI = false, bool SP2 = false>
; __device__ __forceinline__ void gemm_phase(PG8_LAS unsigned char* lds, const Gemm g, const Sched& S, const Epi& E, const bool skip_epi = false) {
;     const int tid = tid_here(), wid = __builtin_amdgcn_readfirstlane(tid >> 6), lane = tid & 63, wr = wid >> 2, wc = wid & 3, fr = lane & 15, fq = lane >> 4;
;     const int K = g.ld, nt = g.K / BK;
;     unsigned voffA[2], voffB[2];
; #pragma unroll
;     for (int i = 0; i < 2; ++i) { int R, C; stage_rc(tid * 16 + i * 8192, R, C); const int Rb = Epi::PERM ? ((R & ~31) + perm32(R & 31)) : R;
;         voffA[i] = (unsigned)(R * K + C) * 2u; voffB[i] = (unsigned)(Rb * K + C) * 2u; }
;     const size_t kstep = (size_t)(BK * 2);
;     const size_t hstep = (size_t)HALF * K * 2;
;     const size_t tstep = 2 * hstep;
;     const size_t pmstepA = Sched::GATHER ? (size_t)0 : tstep;
;     unsigned gA[2][2] = {{0u, 0u}, {0u, 0u}}, gN[2][2] = {{0u, 0u}, {0u, 0u}}; bool last_ = false; (void)gA; (void)gN; (void)last_;
;     ...
;     const unsigned ldsw = (unsigned)wid * 1024u;
;     const int aoff = lds_byte(wr * 64 + fr, fq * 8), boff = lds_byte(wc * 32 + fr, fq * 8);
;     ...
;     Unit cur, nxt; int ui = 0;
;     if (!S.next(0, cur)) return;
;     f32x4 acc[2][2][4][2];
; #pragma unroll
;     for (int a = 0; a < 2; ++a)
; #pragma unroll
;         for (int b = 0; b < 2; ++b)
; #pragma unroll
;             for (int m = 0; m < 4; ++m)
; #pragma unroll
;                 for (int n = 0; n < 2; ++n) acc[a][b][m][n] = (f32x4){0.f, 0.f, 0.f, 0.f};
;     bf16x8 At[4][2], B0[2][2], B1[2][2];
;     const char* cA = (const char*)g.A + (size_t)cur.pm * pmstepA + cur.ko; const char* cB = (const char*)g.Bt + (size_t)cur.pn * tstep + cur.ko;
;     S.a_ready(cur);
;     PG8_GIDX(gA, cur.pm);
;     if constexpr (SP2) {
;         PG8_STAGE(PG8_SB(0, 0), cB, voffB); PG8_STAGE(PG8_SB(0, 1), cB + hstep, voffB); PG8_STAGE_A(0, 0, cA, false); PG8_STAGE_A(0, 1, cA, false);
;         if (wr == 1) PG8_BAR;
;         PG8_WAIT_V(2); PG8_BAR;
;         PG8_STAGE(PG8_SB(1, 0), cB + kstep, voffB); PG8_STAGE_A(1, 0, cA + kstep, false); PG8_STAGE(PG8_SB(1, 1), cB + hstep + kstep, voffB);
;         PG8_WAIT_V(6); PG8_BAR;
;     } else {
;         PG8_STAGE(PG8_SB(0, 0), cB, voffB); PG8_STAGE_A(0, 0, cA, false); PG8_STAGE(PG8_SB(0, 1), cB + hstep, voffB); PG8_STAGE_A(0, 1, cA, false);
.LBB0_711:
	v_readlane_b32 s0, v254, 0
	v_readlane_b32 s1, v254, 1
	s_cmp_lt_i32 s0, 7
	s_cselect_b64 s[0:1], -1, 0
	s_and_b64 s[0:1], s[0:1], s[4:5]
	s_andn2_b64 vcc, exec, s[0:1]
	v_readlane_b32 s2, v254, 2
	v_readlane_b32 s3, v254, 3
	s_cbranch_vccnz .LBB0_779
	s_lshr_b32 vcc_lo, s94, 3
	s_cmp_eq_u32 vcc_lo, 0
	s_cbranch_scc1 .Lstg_g3_done
.Lstg_g3_loop:
	s_sleep 5
	s_add_i32 vcc_lo, vcc_lo, -1
	s_cmp_lg_u32 vcc_lo, 0
	s_cbranch_scc1 .Lstg_g3_loop
.Lstg_g3_done:
	s_waitcnt vmcnt(10)
	v_mov_b32_e32 v12, v0
	s_cmpk_gt_i32 s94, 0x57f
	v_readfirstlane_b32 s10, v12
	s_cbranch_scc1 .LBB0_728
	v_lshlrev_b32_e32 v1, 4, v12
	v_add_u32_e32 v2, 0x2000, v1
	v_ashrrev_i32_e32 v3, 31, v2
	v_lshrrev_b32_e32 v3, 22, v3
	v_add_u32_e32 v3, v2, v3
	v_ashrrev_i32_e32 v10, 10, v3
	v_mul_i32_i24_e32 v3, 0x400, v10
	v_sub_u32_e32 v2, v2, v3
	v_lshrrev_b32_e32 v3, 4, v2
	v_bitop3_b32 v2, v3, v2, 32 bitop3:0x6c
	v_ashrrev_i32_e32 v3, 31, v2
	v_lshrrev_b32_e32 v3, 26, v3
	v_add_u32_e32 v3, v2, v3
	v_lshlrev_b32_e32 v4, 3, v10
	v_ashrrev_i32_e32 v11, 6, v3
	v_and_b32_e32 v4, -16, v4
	v_add_u32_e32 v4, v11, v4
	v_and_b32_e32 v5, 3, v11
	s_mov_b32 s3, 0x1fffe0
	v_lshrrev_b32_e32 v6, 2, v4
	v_lshlrev_b32_e32 v7, 1, v4
	v_and_b32_e32 v3, 0xc0, v3
	v_and_or_b32 v5, v4, s3, v5
	v_and_b32_e32 v6, 4, v6
	v_and_b32_e32 v7, 24, v7
	v_sub_u32_e32 v2, v2, v3
	v_mov_b32_e32 v3, 1
	v_or3_b32 v5, v5, v6, v7
	v_lshlrev_b32_e32 v6, 5, v10
	v_ashrrev_i16_sdwa v2, v3, sext(v2) dst_sel:DWORD dst_unused:UNUSED_PAD src0_sel:DWORD src1_sel:BYTE_0
	v_and_b32_e32 v6, 32, v6
	v_bfe_i32 v13, v2, 0, 16
	v_add_lshl_u32 v2, v6, v13, 1
	v_lshl_add_u32 v142, v5, 11, v2
	v_lshl_add_u32 v144, v4, 11, v2
	v_bfe_i32 v2, v12, 27, 1
	v_lshrrev_b32_e32 v2, 22, v2
	v_add_u32_e32 v2, v1, v2
	v_and_b32_e32 v2, 0xfffffc00, v2
	v_sub_u32_e32 v1, v1, v2
	v_lshrrev_b32_e32 v2, 4, v1
	v_bitop3_b32 v2, v2, v1, 32 bitop3:0x6c
	v_ashrrev_i32_e32 v1, 31, v1
	v_lshrrev_b32_e32 v1, 26, v1
	v_add_u32_e32 v1, v2, v1
	s_waitcnt vmcnt(9)
	v_ashrrev_i32_e32 v14, 6, v1
	v_ashrrev_i32_e32 v1, 31, v12
	v_lshrrev_b32_e32 v1, 26, v1
	v_add_u32_e32 v1, v12, v1
	v_ashrrev_i32_e32 v15, 6, v1
	v_lshlrev_b32_e32 v1, 3, v15
	v_and_b32_e32 v1, -16, v1
	v_add_u32_e32 v1, v14, v1
	v_and_b32_e32 v4, 3, v14
	v_and_or_b32 v4, v1, s3, v4
	s_ashr_i32 s3, s94, 31
	s_lshr_b32 s4, s3, 29
	s_add_i32 s4, s94, s4
	s_ashr_i32 s8, s10, 6
	s_ashr_i32 s6, s4, 3
	s_and_b32 s4, s4, -8
	s_ashr_i32 s5, s10, 8
	s_lshl_b32 s2, s8, 10
	s_sub_i32 s4, s94, s4
	s_cmp_lt_i32 s4, 0
	s_movk_i32 s28, 0xb1
	s_cselect_b32 s7, s28, 0xb0
	s_mul_i32 s4, s7, s4
	s_add_i32 s4, s4, s6
	s_mul_hi_i32 s6, s4, 0x2e8ba2e9
	s_lshr_b32 s7, s6, 31
	s_ashr_i32 s6, s6, 5
	s_add_i32 s6, s6, s7
	s_lshl_b32 s7, s6, 3
	s_mulk_i32 s6, 0xb0
	s_sub_i32 s6, s4, s6
	s_sext_i32_i16 s4, s6
	s_bfe_u32 s4, s4, 0x3001c
	s_add_i32 s9, s6, s4
	s_sext_i32_i16 s4, s9
	s_and_b32 s9, s9, 0xfff8
	v_lshrrev_b32_e32 v5, 2, v1
	v_lshlrev_b32_e32 v6, 1, v1
	s_sub_i32 s6, s6, s9
	v_and_b32_e32 v5, 4, v5
	v_and_b32_e32 v6, 24, v6
	s_sext_i32_i16 s6, s6
	v_or3_b32 v4, v4, v5, v6
	v_mul_i32_i24_e32 v6, 64, v14
	s_lshr_b32 s4, s4, 3
	s_add_i32 s20, s7, s6
	v_sub_u32_e32 v2, v2, v6
	s_ashr_i32 s21, s20, 31
	s_bfe_i64 s[12:13], s[4:5], 0x100000
	v_lshlrev_b32_e32 v5, 5, v15
	v_ashrrev_i16_sdwa v2, v3, sext(v2) dst_sel:DWORD dst_unused:UNUSED_PAD src0_sel:DWORD src1_sel:BYTE_0
	s_lshl_b64 s[6:7], s[20:21], 19
	s_lshl_b64 s[12:13], s[12:13], 19
	v_readlane_b32 s14, v254, 15
	v_and_b32_e32 v5, 32, v5
	v_bfe_i32 v16, v2, 0, 16
	v_readlane_b32 s15, v254, 16
	s_add_u32 s24, s14, s12
	v_add_lshl_u32 v2, v5, v16, 1
	s_addc_u32 s25, s15, s13
	s_add_i32 s29, s2, 0
	v_lshl_add_u32 v146, v4, 11, v2
	s_add_i32 m0, s29, 0x10000
	v_lshl_add_u32 v148, v1, 11, v2
	global_load_lds_dwordx4 v146, s[24:25]
	s_add_i32 m0, s29, 0x12000
	s_add_u32 s12, s24, 0x40000
	global_load_lds_dwordx4 v142, s[24:25]
	s_addc_u32 s13, s25, 0
	s_add_i32 m0, s29, 0x14000
	v_mov_b32_e32 v147, 0
	global_load_lds_dwordx4 v146, s[12:13]
	s_add_i32 m0, s29, 0x16000
	s_add_u32 s22, s86, s6
	s_addc_u32 s23, s87, s7
	s_add_i32 s30, s29, 0x2000
	global_load_lds_dwordx4 v142, s[12:13]
	s_mov_b32 m0, s29
	s_add_u32 s6, s22, 0x40000
	global_load_lds_dwordx4 v148, s[22:23]
	s_mov_b32 m0, s30
	s_addc_u32 s7, s23, 0
	s_add_i32 s31, s29, 0x4000
	global_load_lds_dwordx4 v144, s[22:23]
	s_mov_b32 m0, s31
	s_add_i32 s34, s29, 0x6000
	global_load_lds_dwordx4 v148, s[6:7]
	s_mov_b32 m0, s34
	v_mov_b32_e32 v143, v147
	global_load_lds_dwordx4 v144, s[6:7]
	v_mov_b32_e32 v149, v147
	v_mov_b32_e32 v145, v147
	s_cmp_eq_u32 s5, 1
	s_mov_b32 s35, 0
	v_lshl_add_u64 v[8:9], s[24:25], 0, v[146:147]
	v_lshl_add_u64 v[6:7], s[24:25], 0, v[142:143]
	v_lshl_add_u64 v[2:3], s[22:23], 0, v[148:149]
	s_cselect_b64 s[6:7], -1, 0
	s_cmp_lg_u32 s5, 1
	v_lshl_add_u64 v[4:5], s[22:23], 0, v[144:145]
	s_cbranch_scc1 .LBB0_715
	s_barrier

; template <int layer> __device__ __forceinline__ void layer_phases(const Ctx& c, unsigned char* lds) {
;     ...
;             if (IN(pb + 7)) {
;                 pg8::Gemm g{XB, WE13, MAXROWS, 2 * FE, D, D}; pg8::MoeGatherOrder S{PANE, PANE[MAXPAN], 28, 4, G, bx, ROWSRC};
;                 pg8::EpiGlu<true> E{HE, FE, ROWRS};
;                 pg8::gemm_phase<pg8::EpiGlu<true>, pg8::MoeGatherOrder, true, true>(ldsl, g, S, E, noepi);
.LBB0_1708:
	v_readlane_b32 s8, v254, 0
	s_cmp_lt_i32 s8, 25
	v_readlane_b32 s9, v254, 1
	s_cselect_b64 s[2:3], -1, 0
	s_and_b64 s[8:9], s[2:3], s[4:5]
	s_andn2_b64 vcc, exec, s[8:9]
	v_readlane_b32 s10, v254, 2
	v_readlane_b32 s11, v254, 3
	s_cbranch_vccnz .LBB0_1747
	s_lshr_b32 vcc_lo, s94, 3
	s_cmp_eq_u32 vcc_lo, 0
	s_cbranch_scc1 .Lstg_g5_done

;     __device__ bool next(int i, Unit& u) const {
;         const int nwg = npan * NT; const long L = (long)i * G + c; if (L >= nwg) return false;
;         int wgid = (int)L; { const int q = nwg / NXCD, r = nwg % NXCD, xcd = wgid % NXCD, off = wgid / NXCD; wgid = (xcd < r ? xcd * (q + 1) : r * (q + 1) + (xcd - r) * q) + off; }
; template <int layer> __device__ __forceinline__ void layer_phases(const Ctx& c, unsigned char* lds) {
;     ...
;                 pg8::Gemm g{XB, WE13, MAXROWS, 2 * FE, D, D}; pg8::MoeGatherOrder S{PANE, PANE[MAXPAN], 28, 4, G, bx, ROWSRC};
.Lstg_g5_done:
	v_mov_b32_e32 v131, 0
	global_load_dword v1, v131, s[12:13]
	s_waitcnt vmcnt(12)
	v_mov_b32_e32 v6, v0
	s_waitcnt vmcnt(0)
	v_readfirstlane_b32 s2, v1
	s_mul_i32 s4, s2, 28
	s_cmp_ge_i32 s94, s4
	v_readfirstlane_b32 s26, v6
	s_cbranch_scc1 .LBB0_1735
	s_ashr_i32 s5, s4, 31
	s_lshr_b32 s3, s5, 29
	s_add_i32 s6, s4, s3
	s_ashr_i32 s3, s6, 3
	s_and_b32 s6, s6, -8
	s_ashr_i32 s47, s94, 31
	s_sub_i32 s46, s4, s6
	s_lshr_b32 s6, s47, 29
	s_add_i32 s11, s94, s6
	s_and_b32 s6, s11, -8
	s_sub_i32 s22, s94, s6
	s_add_i32 s48, s3, 1
	s_cmp_ge_i32 s22, s46
	s_mul_i32 s49, s48, s46
	s_cbranch_scc0 .LBB0_1712
	s_sub_i32 s6, s22, s46
	s_mul_i32 s6, s6, s3
	s_add_i32 s10, s6, s49
	s_cbranch_execz .LBB0_1713
	s_branch .LBB0_1714
